# P5 head loop: count the z-piece wait (vmcnt 19 instead of the merged vmcnt 1) so the next-head prefetch stays in flight under the PV MFMAs and epilogue
# speedup vs baseline: 1.1038x; 1.1038x over previous
.LBB0_574:
	s_and_b64 s[6:7], s[90:91], exec
	s_mov_b32 s6, 0xec00
	s_cselect_b32 s6, 0x17400, s6
	s_add_i32 s6, s6, 0
	v_add3_u32 v130, s6, v162, v222
	ds_read_b128 v[94:97], v130
	ds_read_b128 v[98:101], v130 offset:64
	ds_read_b128 v[102:105], v130 offset:4352
	ds_read_b128 v[106:109], v130 offset:4416
	ds_read_b128 v[132:135], v130 offset:8704
	ds_read_b128 v[136:139], v130 offset:8768
	ds_read_b128 v[144:147], v130 offset:13056
	ds_read_b128 v[148:151], v130 offset:13120
	s_waitcnt lgkmcnt(7)
	v_mfma_f32_16x16x32_bf16 v[94:97], v[94:97], v[22:25], 0
	s_waitcnt lgkmcnt(5)
	v_mfma_f32_16x16x32_bf16 v[102:105], v[102:105], v[22:25], 0
	s_waitcnt lgkmcnt(3)
	v_mfma_f32_16x16x32_bf16 v[132:135], v[132:135], v[22:25], 0
	s_waitcnt lgkmcnt(1)
	v_mfma_f32_16x16x32_bf16 v[144:147], v[144:147], v[22:25], 0
	ds_read_b128 v[152:155], v130 offset:128
	ds_read_b128 v[186:189], v130 offset:4480
	ds_read_b128 v[190:193], v130 offset:8832
	ds_read_b128 v[194:197], v130 offset:13184
	v_mfma_f32_16x16x32_bf16 v[94:97], v[98:101], v[26:29], v[94:97]
	v_mfma_f32_16x16x32_bf16 v[98:101], v[106:109], v[26:29], v[102:105]
	s_waitcnt lgkmcnt(4)
	v_mfma_f32_16x16x32_bf16 v[106:109], v[148:151], v[26:29], v[144:147]
	v_mfma_f32_16x16x32_bf16 v[102:105], v[136:139], v[26:29], v[132:135]
	s_nop 2
	ds_read_b128 v[132:135], v130 offset:192
	ds_read_b128 v[136:139], v130 offset:4544
	ds_read_b128 v[144:147], v130 offset:8896
	ds_read_b128 v[148:151], v130 offset:13248
	s_waitcnt lgkmcnt(7)
	v_mfma_f32_16x16x32_bf16 v[94:97], v[152:155], v[30:33], v[94:97]
	s_waitcnt lgkmcnt(6)
	v_mfma_f32_16x16x32_bf16 v[98:101], v[186:189], v[30:33], v[98:101]
	s_waitcnt lgkmcnt(4)
	v_mfma_f32_16x16x32_bf16 v[106:109], v[194:197], v[30:33], v[106:109]
	v_mfma_f32_16x16x32_bf16 v[152:155], v[190:193], v[30:33], v[102:105]
	s_waitcnt lgkmcnt(3)
	v_mfma_f32_16x16x32_bf16 v[132:135], v[132:135], v[34:37], v[94:97]
	s_waitcnt lgkmcnt(2)
	v_mfma_f32_16x16x32_bf16 v[102:105], v[136:139], v[34:37], v[98:101]
	s_waitcnt lgkmcnt(1)
	v_mfma_f32_16x16x32_bf16 v[98:101], v[144:147], v[34:37], v[152:155]
	s_waitcnt lgkmcnt(0)
	v_mfma_f32_16x16x32_bf16 v[94:97], v[148:151], v[34:37], v[106:109]
	s_nop 2
	v_mul_f32_e32 v106, 0x3fb8aa3b, v131
	s_cmpk_eq_i32 s0, 0x700
	s_cbranch_scc1 .Lp5_zw_last
	s_waitcnt vmcnt(19)
	s_branch .Lp5_zw_done
.Lp5_zw_last:
	s_waitcnt vmcnt(1)
.Lp5_zw_done:
	v_lshlrev_b32_e32 v108, 16, v74
	v_exp_f32_e32 v107, v106
	v_mul_f32_e32 v106, 0xbfb8aa3b, v108
	v_exp_f32_e32 v106, v106
	v_mov_b32_e32 v109, v132
	v_and_b32_e32 v132, 0xffff0000, v74
	v_mul_f32_e32 v74, 0xbfb8aa3b, v132
	v_add_f32_e32 v106, 1.0, v106
	v_exp_f32_e32 v74, v74
	v_rcp_f32_e32 v106, v106
	s_cmp_gt_u32 s2, 3
	s_cselect_b64 s[6:7], -1, 0
	v_add_f32_e32 v74, 1.0, v74
	v_pk_mul_f32 v[108:109], v[106:107], v[108:109]
	v_rcp_f32_e32 v106, v74
	v_add_f32_e32 v90, v90, v109
	v_mul_f32_e32 v90, v108, v90
	s_cmp_lt_u32 s2, 2
	v_pk_mul_f32 v[108:109], v[106:107], v[132:133]
	s_cselect_b64 s[88:89], -1, 0
	v_add_f32_e32 v74, v91, v109
	v_mul_f32_e32 v91, v108, v74
	v_lshlrev_b32_e32 v108, 16, v75
	v_mul_f32_e32 v74, 0xbfb8aa3b, v108
	v_exp_f32_e32 v74, v74
	v_mov_b32_e32 v109, v134
	v_and_b32_e32 v134, 0xffff0000, v75
	s_mov_b64 s[8:9], -1
	v_add_f32_e32 v74, 1.0, v74
	v_rcp_f32_e32 v106, v74
	s_and_b64 vcc, exec, s[6:7]
	v_pk_mul_f32 v[108:109], v[106:107], v[108:109]
	s_nop 0
	v_add_f32_e32 v74, v92, v109
	v_mul_f32_e32 v92, v108, v74
	v_mul_f32_e32 v74, 0xbfb8aa3b, v134
	v_exp_f32_e32 v74, v74
	v_lshlrev_b32_e32 v108, 16, v76
	v_mov_b32_e32 v109, v102
	v_and_b32_e32 v102, 0xffff0000, v76
	v_add_f32_e32 v74, 1.0, v74
	v_rcp_f32_e32 v106, v74
	v_mul_f32_e32 v76, 0xbfb8aa3b, v102
	v_exp_f32_e32 v76, v76
	v_pk_mul_f32 v[74:75], v[106:107], v[134:135]
	v_mul_f32_e32 v106, 0xbfb8aa3b, v108
	v_exp_f32_e32 v106, v106
	v_add_f32_e32 v76, 1.0, v76
	v_add_f32_e32 v75, v93, v75
	v_mul_f32_e32 v93, v74, v75
	v_add_f32_e32 v106, 1.0, v106
	v_rcp_f32_e32 v106, v106
	v_cvt_pk_bf16_f32 v74, v90, v91
	v_cvt_pk_bf16_f32 v75, v92, v93
	s_nop 0
	v_pk_mul_f32 v[108:109], v[106:107], v[108:109]
	v_rcp_f32_e32 v106, v76
	v_add_f32_e32 v86, v86, v109
	v_mul_f32_e32 v86, v108, v86
	v_pk_mul_f32 v[102:103], v[106:107], v[102:103]
	s_nop 0
	v_add_f32_e32 v76, v87, v103
	v_mul_f32_e32 v87, v102, v76
	v_lshlrev_b32_e32 v102, 16, v77
	v_mul_f32_e32 v76, 0xbfb8aa3b, v102
	v_exp_f32_e32 v76, v76
	v_mov_b32_e32 v103, v104
	v_and_b32_e32 v104, 0xffff0000, v77
	v_add_f32_e32 v76, 1.0, v76
	v_rcp_f32_e32 v106, v76
	s_nop 0
	v_pk_mul_f32 v[102:103], v[106:107], v[102:103]
	s_nop 0
	v_add_f32_e32 v76, v88, v103
	v_mul_f32_e32 v88, v102, v76
	v_mul_f32_e32 v76, 0xbfb8aa3b, v104
	v_exp_f32_e32 v76, v76
	s_nop 0
	v_add_f32_e32 v76, 1.0, v76
	v_rcp_f32_e32 v106, v76
	s_nop 0
	v_pk_mul_f32 v[76:77], v[106:107], v[104:105]
	s_nop 0
	v_add_f32_e32 v77, v89, v77
	v_mul_f32_e32 v89, v76, v77
	v_cvt_pk_bf16_f32 v76, v86, v87
	v_cvt_pk_bf16_f32 v77, v88, v89
	s_cbranch_vccz .LBB0_576
	v_add_co_u32_e32 v102, vcc, 0x66100000, v128
	s_mov_b64 s[8:9], 0
	s_nop 0
	v_addc_co_u32_e32 v103, vcc, 0, v129, vcc
	global_store_dwordx4 v[102:103], v[74:77], off
